# V table bytes stored as signed 16*hi+lo; sweep V hi-nibble dots take raw bytes (8 fewer VALU per batch), exact correction once per pass
# speedup vs baseline: 1.0714x; 1.0051x over previous
; __device__ __forceinline__ unsigned q4(float x) { return (unsigned)(int)fminf(fmaxf(rintf(x), -7.0f), 7.0f) & 0xfu; }
; __device__ __forceinline__ void cvt_table_i4(const float* src, unsigned char* dst, float* scl, float scl_mul, int gw, int ngw, int lane) {
;     for (int row = gw; row < 16384; row += ngw) {
;         const f32x4* sp = (const f32x4*)(src + (size_t)row * 1024 + 16 * lane);
;         const f32x4 a0 = sp[0], a1 = sp[1], a2 = sp[2], a3 = sp[3];
;         float ss = ((a0.x * a0.x + a0.y * a0.y) + (a0.z * a0.z + a0.w * a0.w)) + ((a1.x * a1.x + a1.y * a1.y) + (a1.z * a1.z + a1.w * a1.w))
;                  + ((a2.x * a2.x + a2.y * a2.y) + (a2.z * a2.z + a2.w * a2.w)) + ((a3.x * a3.x + a3.y * a3.y) + (a3.z * a3.z + a3.w * a3.w));
;         ss = wave_sum(ss);
;         const float step = fmaxf(0.35f * sqrtf(ss * (1.0f / 1024.0f)), 1e-30f), q = 1.0f / step;
;         v2u o;
;         o.x = (q4(a0.x * q) | (q4(a1.x * q) << 4)) | ((q4(a0.y * q) | (q4(a1.y * q) << 4)) << 8) | ((q4(a0.z * q) | (q4(a1.z * q) << 4)) << 16) | ((q4(a0.w * q) | (q4(a1.w * q) << 4)) << 24);
;         o.y = (q4(a2.x * q) | (q4(a3.x * q) << 4)) | ((q4(a2.y * q) | (q4(a3.y * q) << 4)) << 8) | ((q4(a2.z * q) | (q4(a3.z * q) << 4)) << 16) | ((q4(a2.w * q) | (q4(a3.w * q) << 4)) << 24);
;         *(v2u*)(dst + (size_t)row * 512 + 8 * lane) = o;
;         if (lane == 0) scl[row] = step * scl_mul;
;     }
; }
.LBB0_1973:
	global_load_dwordx4 v[8:11], v[4:5], off offset:-32
	global_load_dwordx4 v[12:15], v[4:5], off offset:-16
	global_load_dwordx4 v[20:23], v[4:5], off
	global_load_dwordx4 v[24:27], v[4:5], off offset:16
	s_waitcnt vmcnt(0)
	v_mul_f32_e32 v7, v9, v9
	v_mul_f32_e32 v16, v11, v11
	v_mul_f32_e32 v17, v13, v13
	v_mul_f32_e32 v28, v15, v15
	v_mul_f32_e32 v29, v21, v21
	v_mul_f32_e32 v30, v23, v23
	v_fmac_f32_e32 v7, v8, v8
	v_fmac_f32_e32 v16, v10, v10
	v_fmac_f32_e32 v17, v12, v12
	v_fmac_f32_e32 v28, v14, v14
	v_mul_f32_e32 v31, v25, v25
	v_mul_f32_e32 v32, v27, v27
	v_fmac_f32_e32 v29, v20, v20
	v_fmac_f32_e32 v30, v22, v22
	v_add_f32_e32 v7, v7, v16
	v_add_f32_e32 v16, v17, v28
	v_fmac_f32_e32 v31, v24, v24
	v_fmac_f32_e32 v32, v26, v26
	v_add_f32_e32 v17, v29, v30
	v_add_f32_e32 v7, v7, v16
	v_add_f32_e32 v28, v31, v32
	v_add_f32_e32 v7, v7, v17
	v_add_f32_e32 v7, v7, v28
	s_nop 1
	v_add_f32_dpp v7, v7, v7 quad_perm:[1,0,3,2] row_mask:0xf bank_mask:0xf bound_ctrl:1
	s_nop 1
	v_add_f32_dpp v7, v7, v7 quad_perm:[2,3,0,1] row_mask:0xf bank_mask:0xf bound_ctrl:1
	s_nop 1
	v_add_f32_dpp v7, v7, v7 row_half_mirror row_mask:0xf bank_mask:0xf bound_ctrl:1
	s_nop 1
	v_add_f32_dpp v7, v7, v7 row_mirror row_mask:0xf bank_mask:0xf bound_ctrl:1
	v_mov_b32_e32 v16, v7
	s_nop 1
	v_permlane16_swap_b32_e32 v7, v16
	v_add_f32 v7, v7, v16
	s_nop 1
	s_nop 0
	v_mov_b32_e32 v16, v7
	s_nop 1
	v_permlane32_swap_b32_e32 v7, v16
	v_add_f32 v7, v7, v16
	s_nop 0
	v_mul_f32_e32 v7, 0x3a800000, v7
	v_mul_f32_e32 v16, 0x4f800000, v7
	v_cmp_gt_f32_e32 vcc, s3, v7
	s_nop 1
	v_cndmask_b32_e32 v7, v7, v16, vcc
	v_sqrt_f32_e32 v16, v7
	s_nop 0
	v_add_u32_e32 v17, -1, v16
	v_add_u32_e32 v28, 1, v16
	v_fma_f32 v29, -v17, v16, v7
	v_fma_f32 v30, -v28, v16, v7
	v_cmp_ge_f32_e64 s[0:1], 0, v29
	s_nop 1
	v_cndmask_b32_e64 v16, v16, v17, s[0:1]
	v_cmp_lt_f32_e64 s[0:1], 0, v30
	s_nop 1
	v_cndmask_b32_e64 v16, v16, v28, s[0:1]
	v_mul_f32_e32 v17, 0x37800000, v16
	v_cndmask_b32_e32 v16, v16, v17, vcc
	v_cmp_class_f32_e32 vcc, v7, v1
	s_nop 1
	v_cndmask_b32_e32 v7, v16, v7, vcc
	v_mul_f32_e32 v7, 0x3eb33333, v7
	v_max_f32_e32 v7, 0xda24260, v7
	v_div_scale_f32 v16, s[0:1], v7, v7, 1.0
	v_rcp_f32_e32 v17, v16
	v_div_scale_f32 v28, vcc, 1.0, v7, 1.0
	v_fma_f32 v29, -v16, v17, 1.0
	v_fmac_f32_e32 v17, v29, v17
	v_mul_f32_e32 v29, v28, v17
	v_fma_f32 v30, -v16, v29, v28
	v_fmac_f32_e32 v29, v30, v17
	v_fma_f32 v16, -v16, v29, v28
	v_div_fmas_f32 v16, v16, v17, v29
	v_div_fixup_f32 v16, v16, v7, 1.0
	v_mul_f32_e32 v8, v8, v16
	v_mul_f32_e32 v9, v9, v16
	v_mul_f32_e32 v10, v10, v16
	v_mul_f32_e32 v11, v11, v16
	v_mul_f32_e32 v12, v12, v16
	v_mul_f32_e32 v13, v13, v16
	v_mul_f32_e32 v14, v14, v16
	v_mul_f32_e32 v15, v15, v16
	v_mul_f32_e32 v20, v20, v16
	v_mul_f32_e32 v21, v21, v16
	v_mul_f32_e32 v22, v22, v16
	v_mul_f32_e32 v23, v23, v16
	v_mul_f32_e32 v24, v24, v16
	v_mul_f32_e32 v25, v25, v16
	v_mul_f32_e32 v26, v26, v16
	v_mul_f32_e32 v27, v27, v16
	v_rndne_f32_e32 v8, v8
	v_rndne_f32_e32 v9, v9
	v_rndne_f32_e32 v10, v10
	v_rndne_f32_e32 v11, v11
	v_rndne_f32_e32 v12, v12
	v_rndne_f32_e32 v13, v13
	v_rndne_f32_e32 v14, v14
	v_rndne_f32_e32 v15, v15
	v_rndne_f32_e32 v20, v20
	v_rndne_f32_e32 v21, v21
	v_rndne_f32_e32 v22, v22
	v_rndne_f32_e32 v23, v23
	v_rndne_f32_e32 v24, v24
	v_rndne_f32_e32 v25, v25
	v_rndne_f32_e32 v26, v26
	v_rndne_f32_e32 v27, v27
	v_med3_f32 v8, v8, s13, v6
	v_med3_f32 v9, v9, s13, v6
	v_med3_f32 v10, v10, s13, v6
	v_med3_f32 v11, v11, s13, v6
	v_med3_f32 v12, v12, s13, v6
	v_med3_f32 v13, v13, s13, v6
	v_med3_f32 v14, v14, s13, v6
	v_med3_f32 v15, v15, s13, v6
	v_med3_f32 v20, v20, s13, v6
	v_med3_f32 v21, v21, s13, v6
	v_med3_f32 v22, v22, s13, v6
	v_med3_f32 v23, v23, s13, v6
	v_med3_f32 v24, v24, s13, v6
	v_med3_f32 v25, v25, s13, v6
	v_med3_f32 v26, v26, s13, v6
	v_med3_f32 v27, v27, s13, v6
	v_fmamk_f32 v8, v12, 0x41800000, v8
	v_fmamk_f32 v20, v24, 0x41800000, v20
	v_fmamk_f32 v9, v13, 0x41800000, v9
	v_fmamk_f32 v21, v25, 0x41800000, v21
	v_fmamk_f32 v10, v14, 0x41800000, v10
	v_fmamk_f32 v22, v26, 0x41800000, v22
	v_fmamk_f32 v11, v15, 0x41800000, v11
	v_fmamk_f32 v23, v27, 0x41800000, v23
	v_cvt_i32_f32_e32 v12, v8
	v_cvt_i32_f32_e32 v13, v20
	v_cvt_i32_f32_sdwa v12, v9 dst_sel:BYTE_1 dst_unused:UNUSED_PRESERVE src0_sel:DWORD
	v_cvt_i32_f32_sdwa v13, v21 dst_sel:BYTE_1 dst_unused:UNUSED_PRESERVE src0_sel:DWORD
	v_cvt_i32_f32_sdwa v12, v10 dst_sel:BYTE_2 dst_unused:UNUSED_PRESERVE src0_sel:DWORD
	v_cvt_i32_f32_sdwa v13, v22 dst_sel:BYTE_2 dst_unused:UNUSED_PRESERVE src0_sel:DWORD
	v_cvt_i32_f32_sdwa v12, v11 dst_sel:BYTE_3 dst_unused:UNUSED_PRESERVE src0_sel:DWORD
	v_cvt_i32_f32_sdwa v13, v23 dst_sel:BYTE_3 dst_unused:UNUSED_PRESERVE src0_sel:DWORD
	s_nop 0
	global_store_dwordx2 v[2:3], v[12:13], off
	s_and_saveexec_b64 s[0:1], s[4:5]
	s_cbranch_execz .LBB0_1972
	v_mul_f32_e32 v7, 0x3d800000, v7
	global_store_dword v19, v7, s[6:7]
	s_branch .LBB0_1972

; #define PE_WAIT4U(S, cntstr) asm volatile("s_waitcnt " cntstr : "+v"(ru4[S][0]), "+v"(ru4[S][1]), "+v"(ru4[S][2]), "+v"(ru4[S][3]) :: "memory")
;     ...
; #pragma unroll
;         for (int q = 0; q < PE_RD; ++q) PE_WAIT4U(q, "vmcnt(0)");
;         PE_FLUSH();
.LBB0_2677:
	v_cvt_f32_i32_e32 v54, v54
	v_cvt_f32_i32_e32 v55, v55
	v_cvt_f32_i32_e32 v56, v56
	v_cvt_f32_i32_e32 v57, v57
	v_cvt_f32_i32_e32 v58, v58
	v_cvt_f32_i32_e32 v59, v59
	v_cvt_f32_i32_e32 v60, v60
	v_cvt_f32_i32_e32 v61, v61
	v_cvt_f32_i32_e32 v62, v62
	v_cvt_f32_i32_e32 v63, v63
	v_cvt_f32_i32_e32 v64, v64
	v_cvt_f32_i32_e32 v65, v65
	v_cvt_f32_i32_e32 v66, v66
	v_cvt_f32_i32_e32 v67, v67
	v_cvt_f32_i32_e32 v68, v68
	v_cvt_f32_i32_e32 v69, v69
	v_cvt_f32_i32_e32 v36, v36
	v_cvt_f32_i32_e32 v37, v37
	v_cvt_f32_i32_e32 v38, v38
	v_cvt_f32_i32_e32 v39, v39
	v_cvt_f32_i32_e32 v40, v40
	v_cvt_f32_i32_e32 v41, v41
	v_cvt_f32_i32_e32 v42, v42
	v_cvt_f32_i32_e32 v43, v43
	v_cvt_f32_i32_e32 v44, v44
	v_cvt_f32_i32_e32 v45, v45
	v_cvt_f32_i32_e32 v46, v46
	v_cvt_f32_i32_e32 v47, v47
	v_cvt_f32_i32_e32 v50, v50
	v_cvt_f32_i32_e32 v51, v51
	v_cvt_f32_i32_e32 v52, v52
	v_cvt_f32_i32_e32 v53, v53
	v_cvt_f32_i32_e32 v20, v20
	v_cvt_f32_i32_e32 v21, v21
	v_cvt_f32_i32_e32 v22, v22
	v_cvt_f32_i32_e32 v23, v23
	v_cvt_f32_i32_e32 v24, v24
	v_cvt_f32_i32_e32 v25, v25
	v_cvt_f32_i32_e32 v26, v26
	v_cvt_f32_i32_e32 v27, v27
	v_cvt_f32_i32_e32 v28, v28
	v_cvt_f32_i32_e32 v29, v29
	v_cvt_f32_i32_e32 v30, v30
	v_cvt_f32_i32_e32 v31, v31
	v_cvt_f32_i32_e32 v32, v32
	v_cvt_f32_i32_e32 v33, v33
	v_cvt_f32_i32_e32 v34, v34
	v_cvt_f32_i32_e32 v35, v35
	v_cvt_f32_i32_e32 v18, v18
	v_cvt_f32_i32_e32 v19, v19
	v_cvt_f32_i32_e32 v16, v16
	v_cvt_f32_i32_e32 v17, v17
	v_cvt_f32_i32_e32 v14, v14
	v_cvt_f32_i32_e32 v15, v15
	v_cvt_f32_i32_e32 v12, v12
	v_cvt_f32_i32_e32 v13, v13
	v_cvt_f32_i32_e32 v10, v10
	v_cvt_f32_i32_e32 v11, v11
	v_cvt_f32_i32_e32 v8, v8
	v_cvt_f32_i32_e32 v9, v9
	v_cvt_f32_i32_e32 v6, v6
	v_cvt_f32_i32_e32 v7, v7
	v_cvt_f32_i32_e32 v4, v4
	v_cvt_f32_i32_e32 v5, v5
	v_fmamk_f32 v58, v54, 0xbd800000, v58
	v_fmamk_f32 v59, v55, 0xbd800000, v59
	v_fmamk_f32 v60, v56, 0xbd800000, v60
	v_fmamk_f32 v61, v57, 0xbd800000, v61
	v_fmamk_f32 v66, v62, 0xbd800000, v66
	v_fmamk_f32 v67, v63, 0xbd800000, v67
	v_fmamk_f32 v68, v64, 0xbd800000, v68
	v_fmamk_f32 v69, v65, 0xbd800000, v69
	v_fmamk_f32 v40, v36, 0xbd800000, v40
	v_fmamk_f32 v41, v37, 0xbd800000, v41
	v_fmamk_f32 v42, v38, 0xbd800000, v42
	v_fmamk_f32 v43, v39, 0xbd800000, v43
	v_fmamk_f32 v50, v44, 0xbd800000, v50
	v_fmamk_f32 v51, v45, 0xbd800000, v51
	v_fmamk_f32 v52, v46, 0xbd800000, v52
	v_fmamk_f32 v53, v47, 0xbd800000, v53
	v_fmamk_f32 v24, v20, 0xbd800000, v24
	v_fmamk_f32 v25, v21, 0xbd800000, v25
	v_fmamk_f32 v26, v22, 0xbd800000, v26
	v_fmamk_f32 v27, v23, 0xbd800000, v27
	v_fmamk_f32 v32, v28, 0xbd800000, v32
	v_fmamk_f32 v33, v29, 0xbd800000, v33
	v_fmamk_f32 v34, v30, 0xbd800000, v34
	v_fmamk_f32 v35, v31, 0xbd800000, v35
	v_fmamk_f32 v14, v18, 0xbd800000, v14
	v_fmamk_f32 v15, v19, 0xbd800000, v15
	v_fmamk_f32 v12, v16, 0xbd800000, v12
	v_fmamk_f32 v13, v17, 0xbd800000, v13
	v_fmamk_f32 v6, v10, 0xbd800000, v6
	v_fmamk_f32 v7, v11, 0xbd800000, v7
	v_fmamk_f32 v4, v8, 0xbd800000, v4
	v_fmamk_f32 v5, v9, 0xbd800000, v5
	v_mul_f32_e32 v54, v121, v54
	v_mul_f32_e32 v55, v121, v55
	v_mul_f32_e32 v56, v121, v56
	v_mul_f32_e32 v57, v121, v57
	v_mul_f32_e32 v58, v121, v58
	v_mul_f32_e32 v59, v121, v59
	v_mul_f32_e32 v60, v121, v60
	v_mul_f32_e32 v61, v121, v61
	v_mul_f32_e32 v62, v121, v62
	v_mul_f32_e32 v63, v121, v63
	v_mul_f32_e32 v64, v121, v64
	v_mul_f32_e32 v65, v121, v65
	v_mul_f32_e32 v66, v121, v66
	v_mul_f32_e32 v67, v121, v67
	v_mul_f32_e32 v68, v121, v68
	v_mul_f32_e32 v69, v121, v69
	v_mul_f32_e32 v36, v120, v36
	v_mul_f32_e32 v37, v120, v37
	v_mul_f32_e32 v38, v120, v38
	v_mul_f32_e32 v39, v120, v39
	v_mul_f32_e32 v40, v120, v40
	v_mul_f32_e32 v41, v120, v41
	v_mul_f32_e32 v42, v120, v42
	v_mul_f32_e32 v43, v120, v43
	v_mul_f32_e32 v44, v120, v44
	v_mul_f32_e32 v45, v120, v45
	v_mul_f32_e32 v46, v120, v46
	v_mul_f32_e32 v47, v120, v47
	v_mul_f32_e32 v50, v120, v50
	v_mul_f32_e32 v51, v120, v51
	v_mul_f32_e32 v52, v120, v52
	v_mul_f32_e32 v53, v120, v53
	v_mul_f32_e32 v20, v119, v20
	v_mul_f32_e32 v21, v119, v21
	v_mul_f32_e32 v22, v119, v22
	v_mul_f32_e32 v23, v119, v23
	v_mul_f32_e32 v24, v119, v24
	v_mul_f32_e32 v25, v119, v25
	v_mul_f32_e32 v26, v119, v26
	v_mul_f32_e32 v27, v119, v27
	v_mul_f32_e32 v28, v119, v28
	v_mul_f32_e32 v29, v119, v29
	v_mul_f32_e32 v30, v119, v30
	v_mul_f32_e32 v31, v119, v31
	v_mul_f32_e32 v32, v119, v32
	v_mul_f32_e32 v33, v119, v33
	v_mul_f32_e32 v34, v119, v34
	v_mul_f32_e32 v35, v119, v35
	v_mul_f32_e32 v18, v117, v18
	v_mul_f32_e32 v19, v117, v19
	v_mul_f32_e32 v16, v117, v16
	v_mul_f32_e32 v17, v117, v17
	v_mul_f32_e32 v14, v117, v14
	v_mul_f32_e32 v15, v117, v15
	v_mul_f32_e32 v12, v117, v12
	v_mul_f32_e32 v13, v117, v13
	v_mul_f32_e32 v10, v117, v10
	v_mul_f32_e32 v11, v117, v11
	v_mul_f32_e32 v8, v117, v8
	v_mul_f32_e32 v9, v117, v9
	v_mul_f32_e32 v6, v117, v6
	v_mul_f32_e32 v7, v117, v7
	v_mul_f32_e32 v4, v117, v4
	v_mul_f32_e32 v5, v117, v5
	v_cvt_f32_i32_e32 v0, v108
	v_cvt_f32_i32_e32 v1, v109
	v_cvt_f32_i32_e32 v2, v106
	v_cvt_f32_i32_e32 v3, v107
	v_cvt_f32_i32_e32 v104, v104
	v_cvt_f32_i32_e32 v105, v105
	v_cvt_f32_i32_e32 v102, v102
	v_cvt_f32_i32_e32 v103, v103
	v_cvt_f32_i32_e32 v100, v100
	v_cvt_f32_i32_e32 v101, v101
	v_cvt_f32_i32_e32 v98, v98
	v_cvt_f32_i32_e32 v99, v99
	v_cvt_f32_i32_e32 v96, v96
	v_cvt_f32_i32_e32 v97, v97
	v_cvt_f32_i32_e32 v94, v94
	v_cvt_f32_i32_e32 v95, v95

.LvC_t0:
	s_mulk_i32 s2, 0x690
	s_lshr_b32 s3, s8, 17
	v_perm_b32 v126, v86, v78, s91
	v_perm_b32 v78, v86, v78, s92
	v_perm_b32 v86, v92, v88, s91
	s_add_i32 s2, s90, s2
	s_and_b32 s3, s3, 0x7ffc
	v_perm_b32 v88, v92, v88, s92
	v_perm_b32 v92, v86, v126, s94
	s_add_i32 s2, s2, s3
	v_perm_b32 v86, v86, v126, s68
	v_perm_b32 v126, v88, v78, s94
	v_perm_b32 v78, v88, v78, s68
	v_lshlrev_b32_e32 v88, 4, v92
	v_mov_b32_e32 v48, s2
	v_and_b32_e32 v88, 0xf0f0f0f0, v88
	v_lshlrev_b32_e32 v127, 4, v86
	v_lshlrev_b32_e32 v128, 4, v126
	v_lshlrev_b32_e32 v129, 4, v78
	ds_read_b32 v48, v48 offset:512
	v_and_b32_e32 v127, 0xf0f0f0f0, v127
	v_and_b32_e32 v128, 0xf0f0f0f0, v128
	v_and_b32_e32 v129, 0xf0f0f0f0, v129
	s_waitcnt lgkmcnt(0)
	v_dot4_i32_i8 v54, v88, v48, v54
	v_dot4_i32_i8 v55, v127, v48, v55
	v_dot4_i32_i8 v56, v128, v48, v56
	v_dot4_i32_i8 v57, v129, v48, v57
	v_dot4_i32_i8 v58, v92, v48, v58
	v_dot4_i32_i8 v59, v86, v48, v59
	v_dot4_i32_i8 v60, v126, v48, v60
	v_dot4_i32_i8 v61, v78, v48, v61
	v_perm_b32 v78, v87, v79, s91
	v_perm_b32 v86, v93, v89, s91
	v_perm_b32 v79, v87, v79, s92
	v_perm_b32 v87, v93, v89, s92
	v_perm_b32 v88, v86, v78, s94
	v_perm_b32 v78, v86, v78, s68
	v_perm_b32 v86, v87, v79, s94
	v_perm_b32 v79, v87, v79, s68
	v_lshlrev_b32_e32 v87, 4, v88
	v_and_b32_e32 v87, 0xf0f0f0f0, v87
	v_lshlrev_b32_e32 v89, 4, v78
	v_lshlrev_b32_e32 v92, 4, v86
	v_lshlrev_b32_e32 v93, 4, v79
	v_and_b32_e32 v89, 0xf0f0f0f0, v89
	v_and_b32_e32 v92, 0xf0f0f0f0, v92
	v_and_b32_e32 v93, 0xf0f0f0f0, v93
	v_dot4_i32_i8 v62, v87, v48, v62
	v_dot4_i32_i8 v63, v89, v48, v63
	v_dot4_i32_i8 v64, v92, v48, v64
	v_dot4_i32_i8 v65, v93, v48, v65
	v_dot4_i32_i8 v66, v88, v48, v66
	v_dot4_i32_i8 v67, v78, v48, v67
	v_dot4_i32_i8 v68, v86, v48, v68
	v_dot4_i32_i8 v69, v79, v48, v69
	s_branch .LBB0_2872
.LvC_t1:
	s_mulk_i32 s2, 0x690
	s_lshr_b32 s3, s8, 17
	v_perm_b32 v126, v86, v78, s91
	v_perm_b32 v78, v86, v78, s92
	v_perm_b32 v86, v92, v88, s91
	s_add_i32 s2, s90, s2
	s_and_b32 s3, s3, 0x7ffc
	v_perm_b32 v88, v92, v88, s92
	v_perm_b32 v92, v86, v126, s94
	s_add_i32 s2, s2, s3
	v_perm_b32 v86, v86, v126, s68
	v_perm_b32 v126, v88, v78, s94
	v_perm_b32 v78, v88, v78, s68
	v_lshlrev_b32_e32 v88, 4, v92
	v_mov_b32_e32 v48, s2
	v_and_b32_e32 v88, 0xf0f0f0f0, v88
	v_lshlrev_b32_e32 v127, 4, v86
	v_lshlrev_b32_e32 v128, 4, v126
	v_lshlrev_b32_e32 v129, 4, v78
	ds_read_b32 v48, v48 offset:512
	v_and_b32_e32 v127, 0xf0f0f0f0, v127
	v_and_b32_e32 v128, 0xf0f0f0f0, v128
	v_and_b32_e32 v129, 0xf0f0f0f0, v129
	s_waitcnt lgkmcnt(0)
	v_dot4_i32_i8 v36, v88, v48, v36
	v_dot4_i32_i8 v37, v127, v48, v37
	v_dot4_i32_i8 v38, v128, v48, v38
	v_dot4_i32_i8 v39, v129, v48, v39
	v_dot4_i32_i8 v40, v92, v48, v40
	v_dot4_i32_i8 v41, v86, v48, v41
	v_dot4_i32_i8 v42, v126, v48, v42
	v_dot4_i32_i8 v43, v78, v48, v43
	v_perm_b32 v78, v87, v79, s91
	v_perm_b32 v86, v93, v89, s91
	v_perm_b32 v79, v87, v79, s92
	v_perm_b32 v87, v93, v89, s92
	v_perm_b32 v88, v86, v78, s94
	v_perm_b32 v78, v86, v78, s68
	v_perm_b32 v86, v87, v79, s94
	v_perm_b32 v79, v87, v79, s68
	v_lshlrev_b32_e32 v87, 4, v88
	v_and_b32_e32 v87, 0xf0f0f0f0, v87
	v_lshlrev_b32_e32 v89, 4, v78
	v_lshlrev_b32_e32 v92, 4, v86
	v_lshlrev_b32_e32 v93, 4, v79
	v_and_b32_e32 v89, 0xf0f0f0f0, v89
	v_and_b32_e32 v92, 0xf0f0f0f0, v92
	v_and_b32_e32 v93, 0xf0f0f0f0, v93
	v_dot4_i32_i8 v44, v87, v48, v44
	v_dot4_i32_i8 v45, v89, v48, v45
	v_dot4_i32_i8 v46, v92, v48, v46
	v_dot4_i32_i8 v47, v93, v48, v47
	v_dot4_i32_i8 v50, v88, v48, v50
	v_dot4_i32_i8 v51, v78, v48, v51
	v_dot4_i32_i8 v52, v86, v48, v52
	v_dot4_i32_i8 v53, v79, v48, v53
	s_branch .LBB0_2872
.LvC_t2:
	s_mulk_i32 s2, 0x690
	s_lshr_b32 s3, s8, 17
	v_perm_b32 v126, v86, v78, s91
	v_perm_b32 v78, v86, v78, s92
	v_perm_b32 v86, v92, v88, s91
	s_add_i32 s2, s90, s2
	s_and_b32 s3, s3, 0x7ffc
	v_perm_b32 v88, v92, v88, s92
	v_perm_b32 v92, v86, v126, s94
	s_add_i32 s2, s2, s3
	v_perm_b32 v86, v86, v126, s68
	v_perm_b32 v126, v88, v78, s94
	v_perm_b32 v78, v88, v78, s68
	v_lshlrev_b32_e32 v88, 4, v92
	v_mov_b32_e32 v48, s2
	v_and_b32_e32 v88, 0xf0f0f0f0, v88
	v_lshlrev_b32_e32 v127, 4, v86
	v_lshlrev_b32_e32 v128, 4, v126
	v_lshlrev_b32_e32 v129, 4, v78
	ds_read_b32 v48, v48 offset:512
	v_and_b32_e32 v127, 0xf0f0f0f0, v127
	v_and_b32_e32 v128, 0xf0f0f0f0, v128
	v_and_b32_e32 v129, 0xf0f0f0f0, v129
	s_waitcnt lgkmcnt(0)
	v_dot4_i32_i8 v20, v88, v48, v20
	v_dot4_i32_i8 v21, v127, v48, v21
	v_dot4_i32_i8 v22, v128, v48, v22
	v_dot4_i32_i8 v23, v129, v48, v23
	v_dot4_i32_i8 v24, v92, v48, v24
	v_dot4_i32_i8 v25, v86, v48, v25
	v_dot4_i32_i8 v26, v126, v48, v26
	v_dot4_i32_i8 v27, v78, v48, v27
	v_perm_b32 v78, v87, v79, s91
	v_perm_b32 v86, v93, v89, s91
	v_perm_b32 v79, v87, v79, s92
	v_perm_b32 v87, v93, v89, s92
	v_perm_b32 v88, v86, v78, s94
	v_perm_b32 v78, v86, v78, s68
	v_perm_b32 v86, v87, v79, s94
	v_perm_b32 v79, v87, v79, s68
	v_lshlrev_b32_e32 v87, 4, v88
	v_and_b32_e32 v87, 0xf0f0f0f0, v87
	v_lshlrev_b32_e32 v89, 4, v78
	v_lshlrev_b32_e32 v92, 4, v86
	v_lshlrev_b32_e32 v93, 4, v79
	v_and_b32_e32 v89, 0xf0f0f0f0, v89
	v_and_b32_e32 v92, 0xf0f0f0f0, v92
	v_and_b32_e32 v93, 0xf0f0f0f0, v93
	v_dot4_i32_i8 v28, v87, v48, v28
	v_dot4_i32_i8 v29, v89, v48, v29
	v_dot4_i32_i8 v30, v92, v48, v30
	v_dot4_i32_i8 v31, v93, v48, v31
	v_dot4_i32_i8 v32, v88, v48, v32
	v_dot4_i32_i8 v33, v78, v48, v33
	v_dot4_i32_i8 v34, v86, v48, v34
	v_dot4_i32_i8 v35, v79, v48, v35
	s_branch .LBB0_2872
.LvC_t3:
	s_mulk_i32 s2, 0x690
	s_lshr_b32 s3, s8, 17
	v_perm_b32 v126, v86, v78, s91
	v_perm_b32 v78, v86, v78, s92
	v_perm_b32 v86, v92, v88, s91
	s_add_i32 s2, s90, s2
	s_and_b32 s3, s3, 0x7ffc
	v_perm_b32 v88, v92, v88, s92
	v_perm_b32 v92, v86, v126, s94
	s_add_i32 s2, s2, s3
	v_perm_b32 v86, v86, v126, s68
	v_perm_b32 v126, v88, v78, s94
	v_perm_b32 v78, v88, v78, s68
	v_lshlrev_b32_e32 v88, 4, v92
	v_mov_b32_e32 v48, s2
	v_and_b32_e32 v88, 0xf0f0f0f0, v88
	v_lshlrev_b32_e32 v127, 4, v86
	v_lshlrev_b32_e32 v128, 4, v126
	v_lshlrev_b32_e32 v129, 4, v78
	ds_read_b32 v48, v48 offset:512
	v_and_b32_e32 v127, 0xf0f0f0f0, v127
	v_and_b32_e32 v128, 0xf0f0f0f0, v128
	v_and_b32_e32 v129, 0xf0f0f0f0, v129
	s_waitcnt lgkmcnt(0)
	v_dot4_i32_i8 v18, v88, v48, v18
	v_dot4_i32_i8 v19, v127, v48, v19
	v_dot4_i32_i8 v16, v128, v48, v16
	v_dot4_i32_i8 v17, v129, v48, v17
	v_dot4_i32_i8 v14, v92, v48, v14
	v_dot4_i32_i8 v15, v86, v48, v15
	v_dot4_i32_i8 v12, v126, v48, v12
	v_dot4_i32_i8 v13, v78, v48, v13
	v_perm_b32 v78, v87, v79, s91
	v_perm_b32 v86, v93, v89, s91
	v_perm_b32 v79, v87, v79, s92
	v_perm_b32 v87, v93, v89, s92
	v_perm_b32 v88, v86, v78, s94
	v_perm_b32 v78, v86, v78, s68
	v_perm_b32 v86, v87, v79, s94
	v_perm_b32 v79, v87, v79, s68
	v_lshlrev_b32_e32 v87, 4, v88
	v_and_b32_e32 v87, 0xf0f0f0f0, v87
	v_lshlrev_b32_e32 v89, 4, v78
	v_lshlrev_b32_e32 v92, 4, v86
	v_lshlrev_b32_e32 v93, 4, v79
	v_and_b32_e32 v89, 0xf0f0f0f0, v89
	v_and_b32_e32 v92, 0xf0f0f0f0, v92
	v_and_b32_e32 v93, 0xf0f0f0f0, v93
	v_dot4_i32_i8 v10, v87, v48, v10
	v_dot4_i32_i8 v11, v89, v48, v11
	v_dot4_i32_i8 v8, v92, v48, v8
	v_dot4_i32_i8 v9, v93, v48, v9
	v_dot4_i32_i8 v6, v88, v48, v6
	v_dot4_i32_i8 v7, v78, v48, v7
	v_dot4_i32_i8 v4, v86, v48, v4
	v_dot4_i32_i8 v5, v79, v48, v5

.LvA_t0:
	s_mulk_i32 s2, 0x690
	s_lshr_b32 s3, s4, 17
	v_perm_b32 v126, v72, v70, s91
	v_perm_b32 v70, v72, v70, s92
	v_perm_b32 v72, v80, v74, s91
	s_add_i32 s2, s90, s2
	s_and_b32 s3, s3, 0x7ffc
	v_perm_b32 v74, v80, v74, s92
	v_perm_b32 v80, v72, v126, s94
	s_add_i32 s2, s2, s3
	v_perm_b32 v72, v72, v126, s68
	v_perm_b32 v126, v74, v70, s94
	v_perm_b32 v70, v74, v70, s68
	v_lshlrev_b32_e32 v74, 4, v80
	v_mov_b32_e32 v48, s2
	v_and_b32_e32 v74, 0xf0f0f0f0, v74
	v_lshlrev_b32_e32 v127, 4, v72
	v_lshlrev_b32_e32 v128, 4, v126
	v_lshlrev_b32_e32 v129, 4, v70
	ds_read_b32 v48, v48 offset:512
	v_and_b32_e32 v127, 0xf0f0f0f0, v127
	v_and_b32_e32 v128, 0xf0f0f0f0, v128
	v_and_b32_e32 v129, 0xf0f0f0f0, v129
	s_waitcnt lgkmcnt(0)
	v_dot4_i32_i8 v54, v74, v48, v54
	v_dot4_i32_i8 v55, v127, v48, v55
	v_dot4_i32_i8 v56, v128, v48, v56
	v_dot4_i32_i8 v57, v129, v48, v57
	v_dot4_i32_i8 v58, v80, v48, v58
	v_dot4_i32_i8 v59, v72, v48, v59
	v_dot4_i32_i8 v60, v126, v48, v60
	v_dot4_i32_i8 v61, v70, v48, v61
	v_perm_b32 v70, v73, v71, s91
	v_perm_b32 v72, v81, v75, s91
	v_perm_b32 v71, v73, v71, s92
	v_perm_b32 v73, v81, v75, s92
	v_perm_b32 v74, v72, v70, s94
	v_perm_b32 v70, v72, v70, s68
	v_perm_b32 v72, v73, v71, s94
	v_perm_b32 v71, v73, v71, s68
	v_lshlrev_b32_e32 v73, 4, v74
	v_and_b32_e32 v73, 0xf0f0f0f0, v73
	v_lshlrev_b32_e32 v75, 4, v70
	v_lshlrev_b32_e32 v80, 4, v72
	v_lshlrev_b32_e32 v81, 4, v71
	v_and_b32_e32 v75, 0xf0f0f0f0, v75
	v_and_b32_e32 v80, 0xf0f0f0f0, v80
	v_and_b32_e32 v81, 0xf0f0f0f0, v81
	v_dot4_i32_i8 v62, v73, v48, v62
	v_dot4_i32_i8 v63, v75, v48, v63
	v_dot4_i32_i8 v64, v80, v48, v64
	v_dot4_i32_i8 v65, v81, v48, v65
	v_dot4_i32_i8 v66, v74, v48, v66
	v_dot4_i32_i8 v67, v70, v48, v67
	v_dot4_i32_i8 v68, v72, v48, v68
	v_dot4_i32_i8 v69, v71, v48, v69
	s_branch .LBB0_2877
.LvA_t1:
	s_mulk_i32 s2, 0x690
	s_lshr_b32 s3, s4, 17
	v_perm_b32 v126, v72, v70, s91
	v_perm_b32 v70, v72, v70, s92
	v_perm_b32 v72, v80, v74, s91
	s_add_i32 s2, s90, s2
	s_and_b32 s3, s3, 0x7ffc
	v_perm_b32 v74, v80, v74, s92
	v_perm_b32 v80, v72, v126, s94
	s_add_i32 s2, s2, s3
	v_perm_b32 v72, v72, v126, s68
	v_perm_b32 v126, v74, v70, s94
	v_perm_b32 v70, v74, v70, s68
	v_lshlrev_b32_e32 v74, 4, v80
	v_mov_b32_e32 v48, s2
	v_and_b32_e32 v74, 0xf0f0f0f0, v74
	v_lshlrev_b32_e32 v127, 4, v72
	v_lshlrev_b32_e32 v128, 4, v126
	v_lshlrev_b32_e32 v129, 4, v70
	ds_read_b32 v48, v48 offset:512
	v_and_b32_e32 v127, 0xf0f0f0f0, v127
	v_and_b32_e32 v128, 0xf0f0f0f0, v128
	v_and_b32_e32 v129, 0xf0f0f0f0, v129
	s_waitcnt lgkmcnt(0)
	v_dot4_i32_i8 v36, v74, v48, v36
	v_dot4_i32_i8 v37, v127, v48, v37
	v_dot4_i32_i8 v38, v128, v48, v38
	v_dot4_i32_i8 v39, v129, v48, v39
	v_dot4_i32_i8 v40, v80, v48, v40
	v_dot4_i32_i8 v41, v72, v48, v41
	v_dot4_i32_i8 v42, v126, v48, v42
	v_dot4_i32_i8 v43, v70, v48, v43
	v_perm_b32 v70, v73, v71, s91
	v_perm_b32 v72, v81, v75, s91
	v_perm_b32 v71, v73, v71, s92
	v_perm_b32 v73, v81, v75, s92
	v_perm_b32 v74, v72, v70, s94
	v_perm_b32 v70, v72, v70, s68
	v_perm_b32 v72, v73, v71, s94
	v_perm_b32 v71, v73, v71, s68
	v_lshlrev_b32_e32 v73, 4, v74
	v_and_b32_e32 v73, 0xf0f0f0f0, v73
	v_lshlrev_b32_e32 v75, 4, v70
	v_lshlrev_b32_e32 v80, 4, v72
	v_lshlrev_b32_e32 v81, 4, v71
	v_and_b32_e32 v75, 0xf0f0f0f0, v75
	v_and_b32_e32 v80, 0xf0f0f0f0, v80
	v_and_b32_e32 v81, 0xf0f0f0f0, v81
	v_dot4_i32_i8 v44, v73, v48, v44
	v_dot4_i32_i8 v45, v75, v48, v45
	v_dot4_i32_i8 v46, v80, v48, v46
	v_dot4_i32_i8 v47, v81, v48, v47
	v_dot4_i32_i8 v50, v74, v48, v50
	v_dot4_i32_i8 v51, v70, v48, v51
	v_dot4_i32_i8 v52, v72, v48, v52
	v_dot4_i32_i8 v53, v71, v48, v53
	s_branch .LBB0_2877
.LvA_t2:
	s_mulk_i32 s2, 0x690
	s_lshr_b32 s3, s4, 17
	v_perm_b32 v126, v72, v70, s91
	v_perm_b32 v70, v72, v70, s92
	v_perm_b32 v72, v80, v74, s91
	s_add_i32 s2, s90, s2
	s_and_b32 s3, s3, 0x7ffc
	v_perm_b32 v74, v80, v74, s92
	v_perm_b32 v80, v72, v126, s94
	s_add_i32 s2, s2, s3
	v_perm_b32 v72, v72, v126, s68
	v_perm_b32 v126, v74, v70, s94
	v_perm_b32 v70, v74, v70, s68
	v_lshlrev_b32_e32 v74, 4, v80
	v_mov_b32_e32 v48, s2
	v_and_b32_e32 v74, 0xf0f0f0f0, v74
	v_lshlrev_b32_e32 v127, 4, v72
	v_lshlrev_b32_e32 v128, 4, v126
	v_lshlrev_b32_e32 v129, 4, v70
	ds_read_b32 v48, v48 offset:512
	v_and_b32_e32 v127, 0xf0f0f0f0, v127
	v_and_b32_e32 v128, 0xf0f0f0f0, v128
	v_and_b32_e32 v129, 0xf0f0f0f0, v129
	s_waitcnt lgkmcnt(0)
	v_dot4_i32_i8 v20, v74, v48, v20
	v_dot4_i32_i8 v21, v127, v48, v21
	v_dot4_i32_i8 v22, v128, v48, v22
	v_dot4_i32_i8 v23, v129, v48, v23
	v_dot4_i32_i8 v24, v80, v48, v24
	v_dot4_i32_i8 v25, v72, v48, v25
	v_dot4_i32_i8 v26, v126, v48, v26
	v_dot4_i32_i8 v27, v70, v48, v27
	v_perm_b32 v70, v73, v71, s91
	v_perm_b32 v72, v81, v75, s91
	v_perm_b32 v71, v73, v71, s92
	v_perm_b32 v73, v81, v75, s92
	v_perm_b32 v74, v72, v70, s94
	v_perm_b32 v70, v72, v70, s68
	v_perm_b32 v72, v73, v71, s94
	v_perm_b32 v71, v73, v71, s68
	v_lshlrev_b32_e32 v73, 4, v74
	v_and_b32_e32 v73, 0xf0f0f0f0, v73
	v_lshlrev_b32_e32 v75, 4, v70
	v_lshlrev_b32_e32 v80, 4, v72
	v_lshlrev_b32_e32 v81, 4, v71
	v_and_b32_e32 v75, 0xf0f0f0f0, v75
	v_and_b32_e32 v80, 0xf0f0f0f0, v80
	v_and_b32_e32 v81, 0xf0f0f0f0, v81
	v_dot4_i32_i8 v28, v73, v48, v28
	v_dot4_i32_i8 v29, v75, v48, v29
	v_dot4_i32_i8 v30, v80, v48, v30
	v_dot4_i32_i8 v31, v81, v48, v31
	v_dot4_i32_i8 v32, v74, v48, v32
	v_dot4_i32_i8 v33, v70, v48, v33
	v_dot4_i32_i8 v34, v72, v48, v34
	v_dot4_i32_i8 v35, v71, v48, v35
	s_branch .LBB0_2877
.LvA_t3:
	s_mulk_i32 s2, 0x690
	s_lshr_b32 s3, s4, 17
	v_perm_b32 v126, v72, v70, s91
	v_perm_b32 v70, v72, v70, s92
	v_perm_b32 v72, v80, v74, s91
	s_add_i32 s2, s90, s2
	s_and_b32 s3, s3, 0x7ffc
	v_perm_b32 v74, v80, v74, s92
	v_perm_b32 v80, v72, v126, s94
	s_add_i32 s2, s2, s3
	v_perm_b32 v72, v72, v126, s68
	v_perm_b32 v126, v74, v70, s94
	v_perm_b32 v70, v74, v70, s68
	v_lshlrev_b32_e32 v74, 4, v80
	v_mov_b32_e32 v48, s2
	v_and_b32_e32 v74, 0xf0f0f0f0, v74
	v_lshlrev_b32_e32 v127, 4, v72
	v_lshlrev_b32_e32 v128, 4, v126
	v_lshlrev_b32_e32 v129, 4, v70
	ds_read_b32 v48, v48 offset:512
	v_and_b32_e32 v127, 0xf0f0f0f0, v127
	v_and_b32_e32 v128, 0xf0f0f0f0, v128
	v_and_b32_e32 v129, 0xf0f0f0f0, v129
	s_waitcnt lgkmcnt(0)
	v_dot4_i32_i8 v18, v74, v48, v18
	v_dot4_i32_i8 v19, v127, v48, v19
	v_dot4_i32_i8 v16, v128, v48, v16
	v_dot4_i32_i8 v17, v129, v48, v17
	v_dot4_i32_i8 v14, v80, v48, v14
	v_dot4_i32_i8 v15, v72, v48, v15
	v_dot4_i32_i8 v12, v126, v48, v12
	v_dot4_i32_i8 v13, v70, v48, v13
	v_perm_b32 v70, v73, v71, s91
	v_perm_b32 v72, v81, v75, s91
	v_perm_b32 v71, v73, v71, s92
	v_perm_b32 v73, v81, v75, s92
	v_perm_b32 v74, v72, v70, s94
	v_perm_b32 v70, v72, v70, s68
	v_perm_b32 v72, v73, v71, s94
	v_perm_b32 v71, v73, v71, s68
	v_lshlrev_b32_e32 v73, 4, v74
	v_and_b32_e32 v73, 0xf0f0f0f0, v73
	v_lshlrev_b32_e32 v75, 4, v70
	v_lshlrev_b32_e32 v80, 4, v72
	v_lshlrev_b32_e32 v81, 4, v71
	v_and_b32_e32 v75, 0xf0f0f0f0, v75
	v_and_b32_e32 v80, 0xf0f0f0f0, v80
	v_and_b32_e32 v81, 0xf0f0f0f0, v81
	v_dot4_i32_i8 v10, v73, v48, v10
	v_dot4_i32_i8 v11, v75, v48, v11
	v_dot4_i32_i8 v8, v80, v48, v8
	v_dot4_i32_i8 v9, v81, v48, v9
	v_dot4_i32_i8 v6, v74, v48, v6
	v_dot4_i32_i8 v7, v70, v48, v7
	v_dot4_i32_i8 v4, v72, v48, v4
	v_dot4_i32_i8 v5, v71, v48, v5

.LvB_t0:
	s_mulk_i32 s2, 0x690
	s_lshr_b32 s3, s5, 17
	v_perm_b32 v126, v82, v76, s91
	v_perm_b32 v76, v82, v76, s92
	v_perm_b32 v82, v90, v84, s91
	s_add_i32 s2, s90, s2
	s_and_b32 s3, s3, 0x7ffc
	v_perm_b32 v84, v90, v84, s92
	v_perm_b32 v90, v82, v126, s94
	s_add_i32 s2, s2, s3
	v_perm_b32 v82, v82, v126, s68
	v_perm_b32 v126, v84, v76, s94
	v_perm_b32 v76, v84, v76, s68
	v_lshlrev_b32_e32 v84, 4, v90
	v_mov_b32_e32 v48, s2
	v_and_b32_e32 v84, 0xf0f0f0f0, v84
	v_lshlrev_b32_e32 v127, 4, v82
	v_lshlrev_b32_e32 v128, 4, v126
	v_lshlrev_b32_e32 v129, 4, v76
	ds_read_b32 v48, v48 offset:512
	v_and_b32_e32 v127, 0xf0f0f0f0, v127
	v_and_b32_e32 v128, 0xf0f0f0f0, v128
	v_and_b32_e32 v129, 0xf0f0f0f0, v129
	s_waitcnt lgkmcnt(0)
	v_dot4_i32_i8 v54, v84, v48, v54
	v_dot4_i32_i8 v55, v127, v48, v55
	v_dot4_i32_i8 v56, v128, v48, v56
	v_dot4_i32_i8 v57, v129, v48, v57
	v_dot4_i32_i8 v58, v90, v48, v58
	v_dot4_i32_i8 v59, v82, v48, v59
	v_dot4_i32_i8 v60, v126, v48, v60
	v_dot4_i32_i8 v61, v76, v48, v61
	v_perm_b32 v76, v83, v77, s91
	v_perm_b32 v82, v91, v85, s91
	v_perm_b32 v77, v83, v77, s92
	v_perm_b32 v83, v91, v85, s92
	v_perm_b32 v84, v82, v76, s94
	v_perm_b32 v76, v82, v76, s68
	v_perm_b32 v82, v83, v77, s94
	v_perm_b32 v77, v83, v77, s68
	v_lshlrev_b32_e32 v83, 4, v84
	v_and_b32_e32 v83, 0xf0f0f0f0, v83
	v_lshlrev_b32_e32 v85, 4, v76
	v_lshlrev_b32_e32 v90, 4, v82
	v_lshlrev_b32_e32 v91, 4, v77
	v_and_b32_e32 v85, 0xf0f0f0f0, v85
	v_and_b32_e32 v90, 0xf0f0f0f0, v90
	v_and_b32_e32 v91, 0xf0f0f0f0, v91
	v_dot4_i32_i8 v62, v83, v48, v62
	v_dot4_i32_i8 v63, v85, v48, v63
	v_dot4_i32_i8 v64, v90, v48, v64
	v_dot4_i32_i8 v65, v91, v48, v65
	v_dot4_i32_i8 v66, v84, v48, v66
	v_dot4_i32_i8 v67, v76, v48, v67
	v_dot4_i32_i8 v68, v82, v48, v68
	v_dot4_i32_i8 v69, v77, v48, v69
	s_branch .LBB0_2881
.LvB_t1:
	s_mulk_i32 s2, 0x690
	s_lshr_b32 s3, s5, 17
	v_perm_b32 v126, v82, v76, s91
	v_perm_b32 v76, v82, v76, s92
	v_perm_b32 v82, v90, v84, s91
	s_add_i32 s2, s90, s2
	s_and_b32 s3, s3, 0x7ffc
	v_perm_b32 v84, v90, v84, s92
	v_perm_b32 v90, v82, v126, s94
	s_add_i32 s2, s2, s3
	v_perm_b32 v82, v82, v126, s68
	v_perm_b32 v126, v84, v76, s94
	v_perm_b32 v76, v84, v76, s68
	v_lshlrev_b32_e32 v84, 4, v90
	v_mov_b32_e32 v48, s2
	v_and_b32_e32 v84, 0xf0f0f0f0, v84
	v_lshlrev_b32_e32 v127, 4, v82
	v_lshlrev_b32_e32 v128, 4, v126
	v_lshlrev_b32_e32 v129, 4, v76
	ds_read_b32 v48, v48 offset:512
	v_and_b32_e32 v127, 0xf0f0f0f0, v127
	v_and_b32_e32 v128, 0xf0f0f0f0, v128
	v_and_b32_e32 v129, 0xf0f0f0f0, v129
	s_waitcnt lgkmcnt(0)
	v_dot4_i32_i8 v36, v84, v48, v36
	v_dot4_i32_i8 v37, v127, v48, v37
	v_dot4_i32_i8 v38, v128, v48, v38
	v_dot4_i32_i8 v39, v129, v48, v39
	v_dot4_i32_i8 v40, v90, v48, v40
	v_dot4_i32_i8 v41, v82, v48, v41
	v_dot4_i32_i8 v42, v126, v48, v42
	v_dot4_i32_i8 v43, v76, v48, v43
	v_perm_b32 v76, v83, v77, s91
	v_perm_b32 v82, v91, v85, s91
	v_perm_b32 v77, v83, v77, s92
	v_perm_b32 v83, v91, v85, s92
	v_perm_b32 v84, v82, v76, s94
	v_perm_b32 v76, v82, v76, s68
	v_perm_b32 v82, v83, v77, s94
	v_perm_b32 v77, v83, v77, s68
	v_lshlrev_b32_e32 v83, 4, v84
	v_and_b32_e32 v83, 0xf0f0f0f0, v83
	v_lshlrev_b32_e32 v85, 4, v76
	v_lshlrev_b32_e32 v90, 4, v82
	v_lshlrev_b32_e32 v91, 4, v77
	v_and_b32_e32 v85, 0xf0f0f0f0, v85
	v_and_b32_e32 v90, 0xf0f0f0f0, v90
	v_and_b32_e32 v91, 0xf0f0f0f0, v91
	v_dot4_i32_i8 v44, v83, v48, v44
	v_dot4_i32_i8 v45, v85, v48, v45
	v_dot4_i32_i8 v46, v90, v48, v46
	v_dot4_i32_i8 v47, v91, v48, v47
	v_dot4_i32_i8 v50, v84, v48, v50
	v_dot4_i32_i8 v51, v76, v48, v51
	v_dot4_i32_i8 v52, v82, v48, v52
	v_dot4_i32_i8 v53, v77, v48, v53
	s_branch .LBB0_2881
.LvB_t2:
	s_mulk_i32 s2, 0x690
	s_lshr_b32 s3, s5, 17
	v_perm_b32 v126, v82, v76, s91
	v_perm_b32 v76, v82, v76, s92
	v_perm_b32 v82, v90, v84, s91
	s_add_i32 s2, s90, s2
	s_and_b32 s3, s3, 0x7ffc
	v_perm_b32 v84, v90, v84, s92
	v_perm_b32 v90, v82, v126, s94
	s_add_i32 s2, s2, s3
	v_perm_b32 v82, v82, v126, s68
	v_perm_b32 v126, v84, v76, s94
	v_perm_b32 v76, v84, v76, s68
	v_lshlrev_b32_e32 v84, 4, v90
	v_mov_b32_e32 v48, s2
	v_and_b32_e32 v84, 0xf0f0f0f0, v84
	v_lshlrev_b32_e32 v127, 4, v82
	v_lshlrev_b32_e32 v128, 4, v126
	v_lshlrev_b32_e32 v129, 4, v76
	ds_read_b32 v48, v48 offset:512
	v_and_b32_e32 v127, 0xf0f0f0f0, v127
	v_and_b32_e32 v128, 0xf0f0f0f0, v128
	v_and_b32_e32 v129, 0xf0f0f0f0, v129
	s_waitcnt lgkmcnt(0)
	v_dot4_i32_i8 v20, v84, v48, v20
	v_dot4_i32_i8 v21, v127, v48, v21
	v_dot4_i32_i8 v22, v128, v48, v22
	v_dot4_i32_i8 v23, v129, v48, v23
	v_dot4_i32_i8 v24, v90, v48, v24
	v_dot4_i32_i8 v25, v82, v48, v25
	v_dot4_i32_i8 v26, v126, v48, v26
	v_dot4_i32_i8 v27, v76, v48, v27
	v_perm_b32 v76, v83, v77, s91
	v_perm_b32 v82, v91, v85, s91
	v_perm_b32 v77, v83, v77, s92
	v_perm_b32 v83, v91, v85, s92
	v_perm_b32 v84, v82, v76, s94
	v_perm_b32 v76, v82, v76, s68
	v_perm_b32 v82, v83, v77, s94
	v_perm_b32 v77, v83, v77, s68
	v_lshlrev_b32_e32 v83, 4, v84
	v_and_b32_e32 v83, 0xf0f0f0f0, v83
	v_lshlrev_b32_e32 v85, 4, v76
	v_lshlrev_b32_e32 v90, 4, v82
	v_lshlrev_b32_e32 v91, 4, v77
	v_and_b32_e32 v85, 0xf0f0f0f0, v85
	v_and_b32_e32 v90, 0xf0f0f0f0, v90
	v_and_b32_e32 v91, 0xf0f0f0f0, v91
	v_dot4_i32_i8 v28, v83, v48, v28
	v_dot4_i32_i8 v29, v85, v48, v29
	v_dot4_i32_i8 v30, v90, v48, v30
	v_dot4_i32_i8 v31, v91, v48, v31
	v_dot4_i32_i8 v32, v84, v48, v32
	v_dot4_i32_i8 v33, v76, v48, v33
	v_dot4_i32_i8 v34, v82, v48, v34
	v_dot4_i32_i8 v35, v77, v48, v35
	s_branch .LBB0_2881
.LvB_t3:
	s_mulk_i32 s2, 0x690
	s_lshr_b32 s3, s5, 17
	v_perm_b32 v126, v82, v76, s91
	v_perm_b32 v76, v82, v76, s92
	v_perm_b32 v82, v90, v84, s91
	s_add_i32 s2, s90, s2
	s_and_b32 s3, s3, 0x7ffc
	v_perm_b32 v84, v90, v84, s92
	v_perm_b32 v90, v82, v126, s94
	s_add_i32 s2, s2, s3
	v_perm_b32 v82, v82, v126, s68
	v_perm_b32 v126, v84, v76, s94
	v_perm_b32 v76, v84, v76, s68
	v_lshlrev_b32_e32 v84, 4, v90
	v_mov_b32_e32 v48, s2
	v_and_b32_e32 v84, 0xf0f0f0f0, v84
	v_lshlrev_b32_e32 v127, 4, v82
	v_lshlrev_b32_e32 v128, 4, v126
	v_lshlrev_b32_e32 v129, 4, v76
	ds_read_b32 v48, v48 offset:512
	v_and_b32_e32 v127, 0xf0f0f0f0, v127
	v_and_b32_e32 v128, 0xf0f0f0f0, v128
	v_and_b32_e32 v129, 0xf0f0f0f0, v129
	s_waitcnt lgkmcnt(0)
	v_dot4_i32_i8 v18, v84, v48, v18
	v_dot4_i32_i8 v19, v127, v48, v19
	v_dot4_i32_i8 v16, v128, v48, v16
	v_dot4_i32_i8 v17, v129, v48, v17
	v_dot4_i32_i8 v14, v90, v48, v14
	v_dot4_i32_i8 v15, v82, v48, v15
	v_dot4_i32_i8 v12, v126, v48, v12
	v_dot4_i32_i8 v13, v76, v48, v13
	v_perm_b32 v76, v83, v77, s91
	v_perm_b32 v82, v91, v85, s91
	v_perm_b32 v77, v83, v77, s92
	v_perm_b32 v83, v91, v85, s92
	v_perm_b32 v84, v82, v76, s94
	v_perm_b32 v76, v82, v76, s68
	v_perm_b32 v82, v83, v77, s94
	v_perm_b32 v77, v83, v77, s68
	v_lshlrev_b32_e32 v83, 4, v84
	v_and_b32_e32 v83, 0xf0f0f0f0, v83
	v_lshlrev_b32_e32 v85, 4, v76
	v_lshlrev_b32_e32 v90, 4, v82
	v_lshlrev_b32_e32 v91, 4, v77
	v_and_b32_e32 v85, 0xf0f0f0f0, v85
	v_and_b32_e32 v90, 0xf0f0f0f0, v90
	v_and_b32_e32 v91, 0xf0f0f0f0, v91
	v_dot4_i32_i8 v10, v83, v48, v10
	v_dot4_i32_i8 v11, v85, v48, v11
	v_dot4_i32_i8 v8, v90, v48, v8
	v_dot4_i32_i8 v9, v91, v48, v9
	v_dot4_i32_i8 v6, v84, v48, v6
	v_dot4_i32_i8 v7, v76, v48, v7
	v_dot4_i32_i8 v4, v82, v48, v4
	v_dot4_i32_i8 v5, v77, v48, v5
